# attention: K/V tile DMA issue split by wave half (waves 4-7 issue after QK MFMAs) + P7 epilogue batching
# baseline (speedup 1.0000x reference)
; __device__ __forceinline__ int v_rd_base(int lane) { return ((lane & 3) << 3) | (((lane >> 2) & 3) << 6) | (((lane >> 4) & 1) << 5) | (((lane >> 5) & 1) << 8); }
; __device__ __forceinline__ void block(const Blk& B, char* lds, A3_LAS unsigned char* ldsl, const int tid) {
;     const int wid = __builtin_amdgcn_readfirstlane(tid >> 6), lane = tid & 63, r32 = lane & 31, hi = lane >> 5;
;     const int NT = (B.P0 + QB3) / 64;
;     char* K_lds = lds + KOFF; char* V_lds = lds + VOFF;
;     float* sc_l = (float*)(lds + SCOFF) + wid * 64;
;     const int vb0 = (int)(uintptr_t)V_lds + attn::v_rd_base(lane);
;     const int qlo = B.P0 + wid * 32, qm = qlo + r32 - 4 * hi;
;     constexpr float C2 = 1.4426950408889634f * attn::SCALE;
;     unsigned kso[2], vso[2];
; #pragma unroll
;     for (int i = 0; i < 2; ++i) { const int row = (2 * wid + i) * 4 + (lane >> 4); const int c = (lane & 15) ^ (row & 7); kso[i] = (unsigned)(row * 128 + c * 8) * 2u; }
; #pragma unroll
;     for (int q = 0; q < 2; ++q) { const int st = 2 * (2 * wid + q) + (lane >> 5), w16 = lane & 31; const int k = (st >> 2) * 8 + (w16 >> 2);
;         const int c = (st & 3) * 32 + (w16 & 3) * 8; vso[q] = (unsigned)(k * 128 + c) * 2u; }
;     ...
;     float m_reg = -1e30f, l_reg = 0.f; bf16x8 qr[8]; f32x16 o[8] = {};
; #pragma unroll
;     for (int d0 = 0; d0 < 8; ++d0) qr[d0] = attn::load8<abf>(B.Q + (size_t)(wid * 32 + r32) * 128 + d0 * 16 + hi * 8);
;     A3_STAGE(0, 0);
;     asm volatile("s_waitcnt vmcnt(0)" ::: "memory");
;     __syncthreads();
.LBB0_323:
	s_cmp_eq_u32 s4, s94
	s_cselect_b32 s6, s95, s93
	s_lshl_b32 s17, s6, 8
	s_lshl_b32 s2, s6, 16
	v_mbcnt_lo_u32_b32 v197, -1, 0
	v_mbcnt_hi_u32_b32 v197, -1, v197
	s_add_u32 s2, s96, s2
	v_add_u32_e32 v0, s33, v197
	s_addc_u32 s3, s97, 0
	v_readfirstlane_b32 s4, v0
	s_ashr_i32 s5, s4, 6
	v_bfe_u32 v0, v197, 4, 2
	s_waitcnt vmcnt(23)
	v_lshl_or_b32 v2, s5, 3, v0
	v_bitop3_b32 v0, v0, v197, 15 bitop3:0x78
	v_lshlrev_b32_e32 v0, 4, v0
	v_and_b32_e32 v3, 15, v197
	v_lshl_or_b32 v199, v2, 8, v0
	v_or_b32_e32 v0, 4, v2
	v_bitop3_b32 v2, v0, v3, 7 bitop3:0x6c
	v_lshlrev_b32_e32 v0, 8, v0
	s_waitcnt vmcnt(21)
	v_lshlrev_b32_e32 v6, 3, v197
	v_lshl_or_b32 v200, v2, 4, v0
	v_and_b32_e32 v0, 24, v6
	v_lshlrev_b32_e32 v2, 5, v197
	v_and_b32_e32 v196, 31, v197
	s_lshl_b32 s56, s5, 5
	v_and_or_b32 v0, v197, 32, v0
	s_lshl_b32 s19, s5, 10
	v_and_b32_e32 v2, 0x380, v2
	v_or3_b32 v0, s19, v2, v0
	v_or_b32_e32 v2, s56, v196
	v_ashrrev_i32_e32 v3, 31, v2
	v_bfe_u32 v198, v197, 5, 1
	v_lshlrev_b64 v[4:5], 8, v[2:3]
	v_lshlrev_b32_e32 v201, 1, v0
	v_lshl_add_u64 v[4:5], s[2:3], 0, v[4:5]
	v_lshlrev_b32_e32 v0, 4, v198
	v_lshl_add_u64 v[4:5], v[4:5], 0, v[0:1]
	s_lshl_b32 s2, s5, 11
	v_or_b32_e32 v202, 0x80, v201
	global_load_dwordx4 v[162:165], v[4:5], off
	global_load_dwordx4 v[166:169], v[4:5], off offset:32
	global_load_dwordx4 v[170:173], v[4:5], off offset:64
	global_load_dwordx4 v[174:177], v[4:5], off offset:96
	global_load_dwordx4 v[178:181], v[4:5], off offset:128
	global_load_dwordx4 v[182:185], v[4:5], off offset:160
	global_load_dwordx4 v[186:189], v[4:5], off offset:192
	global_load_dwordx4 v[190:193], v[4:5], off offset:224
	s_add_i32 s19, s2, 0
	v_mov_b32_e32 v3, v201
	v_mov_b32_e32 v4, v200
	v_mov_b32_e32 v5, v202
	v_mov_b32_e32 v7, v199
	s_mov_b32 m0, s19
	s_and_b32 s3, s4, 0x3fffffc0
	global_load_lds_dwordx4 v7, s[46:47]
	s_add_i32 m0, s19, 0x400
	s_lshl_b32 s3, s3, 2
	global_load_lds_dwordx4 v4, s[46:47]
	s_add_i32 m0, s19, 0x8000
	s_add_i32 s2, s17, 0x100
	global_load_lds_dwordx4 v3, s[48:49]
	s_add_i32 m0, s19, 0xc000
	s_add_i32 s3, s3, 0
	global_load_lds_dwordx4 v3, s[50:51]
	s_add_i32 m0, s19, 0x8400
	s_add_i32 s4, s3, 0x18000
	global_load_lds_dwordx4 v5, s[48:49]
	s_add_i32 m0, s19, 0xc400
	s_add_i32 s23, s56, s17
	global_load_lds_dwordx4 v5, s[50:51]
	s_lshr_b32 s57, s2, 6
	v_lshlrev_b32_e32 v5, 4, v197
	v_lshlrev_b32_e32 v8, 1, v197
	s_movk_i32 s2, 0x70
	v_and_b32_e32 v8, 32, v8
	v_and_b32_e32 v9, 0x70, v5
	v_bitop3_b32 v206, v0, v5, s2 bitop3:0x78
	s_movk_i32 s2, 0x60
	v_lshl_add_u32 v204, v196, 2, s4
	v_add_u32_e32 v203, s4, v0
	s_movk_i32 s4, 0x118
	s_cmp_lg_u32 0, -1
	v_bitop3_b32 v207, v0, v9, 32 bitop3:0x36
	v_bitop3_b32 v208, v0, v9, 64 bitop3:0x36
	v_bitop3_b32 v209, v0, v9, s2 bitop3:0x36
	v_and_or_b32 v0, v6, s4, v8
	s_cselect_b32 s4, 0, 0
	v_and_b32_e32 v3, 63, v197
	v_lshlrev_b32_e32 v4, 2, v198
	v_and_b32_e32 v7, 0xc0, v5
	s_add_i32 s4, s4, 0x8000
	s_waitcnt vmcnt(0)
	v_mov_b32_e32 v14, v1
	v_mov_b32_e32 v15, v1
	s_waitcnt vmcnt(0)
	v_cmp_gt_u32_e64 s[2:3], 32, v3
	v_add3_u32 v210, v7, s4, v0
	v_sub_u32_e32 v211, v2, v4
	v_mov_b32_e32 v0, v1
	v_mov_b32_e32 v2, v1
	v_mov_b32_e32 v3, v1
	v_mov_b32_e32 v4, v1
	v_mov_b32_e32 v5, v1
	v_mov_b32_e32 v6, v1
	v_mov_b32_e32 v7, v1
	v_mov_b32_e32 v8, v1
	v_mov_b32_e32 v9, v1
	v_mov_b32_e32 v10, v1
	v_mov_b32_e32 v11, v1
	v_mov_b32_e32 v12, v1
	v_mov_b32_e32 v13, v1
	v_mov_b64_e32 v[128:129], v[14:15]
	v_mov_b64_e32 v[112:113], v[14:15]
	v_mov_b64_e32 v[96:97], v[14:15]
	v_mov_b64_e32 v[80:81], v[14:15]
	v_mov_b64_e32 v[64:65], v[14:15]
	v_mov_b64_e32 v[48:49], v[14:15]
	v_mov_b64_e32 v[32:33], v[14:15]
	v_mov_b64_e32 v[126:127], v[12:13]
	v_mov_b64_e32 v[124:125], v[10:11]
	v_mov_b64_e32 v[122:123], v[8:9]
	v_mov_b64_e32 v[120:121], v[6:7]
	v_mov_b64_e32 v[118:119], v[4:5]
	v_mov_b64_e32 v[116:117], v[2:3]
	v_mov_b64_e32 v[114:115], v[0:1]
	v_mov_b64_e32 v[110:111], v[12:13]
	v_mov_b64_e32 v[108:109], v[10:11]
	v_mov_b64_e32 v[106:107], v[8:9]
	v_mov_b64_e32 v[104:105], v[6:7]
	v_mov_b64_e32 v[102:103], v[4:5]
	v_mov_b64_e32 v[100:101], v[2:3]
	v_mov_b64_e32 v[98:99], v[0:1]
	v_mov_b64_e32 v[94:95], v[12:13]
	v_mov_b64_e32 v[92:93], v[10:11]
	v_mov_b64_e32 v[90:91], v[8:9]
	v_mov_b64_e32 v[88:89], v[6:7]
	v_mov_b64_e32 v[86:87], v[4:5]
	v_mov_b64_e32 v[84:85], v[2:3]
	v_mov_b64_e32 v[82:83], v[0:1]
	v_mov_b64_e32 v[78:79], v[12:13]
	v_mov_b64_e32 v[76:77], v[10:11]
	v_mov_b64_e32 v[74:75], v[8:9]
	v_mov_b64_e32 v[72:73], v[6:7]
	v_mov_b64_e32 v[70:71], v[4:5]
	v_mov_b64_e32 v[68:69], v[2:3]
	v_mov_b64_e32 v[66:67], v[0:1]
	v_mov_b64_e32 v[62:63], v[12:13]
	v_mov_b64_e32 v[60:61], v[10:11]
	v_mov_b64_e32 v[58:59], v[8:9]
	v_mov_b64_e32 v[56:57], v[6:7]
	v_mov_b64_e32 v[54:55], v[4:5]
	v_mov_b64_e32 v[52:53], v[2:3]
	v_mov_b64_e32 v[50:51], v[0:1]
	v_mov_b64_e32 v[46:47], v[12:13]
	v_mov_b64_e32 v[44:45], v[10:11]
	v_mov_b64_e32 v[42:43], v[8:9]
	v_mov_b64_e32 v[40:41], v[6:7]
	v_mov_b64_e32 v[38:39], v[4:5]
	v_mov_b64_e32 v[36:37], v[2:3]
	v_mov_b64_e32 v[34:35], v[0:1]
	v_mov_b64_e32 v[30:31], v[12:13]
	v_mov_b64_e32 v[28:29], v[10:11]
	v_mov_b64_e32 v[26:27], v[8:9]
	v_mov_b64_e32 v[24:25], v[6:7]
	v_mov_b64_e32 v[22:23], v[4:5]
	v_mov_b64_e32 v[20:21], v[2:3]
	v_mov_b64_e32 v[18:19], v[0:1]
	v_mov_b64_e32 v[16:17], v[14:15]
	s_mov_b32 s5, 1
	v_lshlrev_b32_e32 v205, 8, v196
	v_mov_b32_e32 v212, 0
	v_mov_b32_e32 v213, 0xf149f2ca
	s_movk_i32 s62, 0xff00
	s_mov_b64 s[58:59], s[28:29]
	v_mov_b64_e32 v[14:15], v[12:13]
	v_mov_b64_e32 v[12:13], v[10:11]
	v_mov_b64_e32 v[10:11], v[8:9]
	v_mov_b64_e32 v[8:9], v[6:7]
	v_mov_b64_e32 v[6:7], v[4:5]
	v_mov_b64_e32 v[4:5], v[2:3]
	v_mov_b64_e32 v[2:3], v[0:1]
	s_waitcnt vmcnt(0) lgkmcnt(0)
	s_barrier
; __device__ __forceinline__ void block(const Blk& B, char* lds, A3_LAS unsigned char* ldsl, const int tid) {
;     ...
;     for (int t = 0; t < NT; ++t) {
;         const int buf = t & 1, kb = t * 64;
;         if (t + 1 < NT) A3_STAGE(t + 1, buf ^ 1);
;         f32x16 p0, p1;
;         attn::qkt<0, false>(p0, p1, K_lds + buf * 16384, r32, hi, qr, true);
;         if (kb + 63 > qlo) attn::mask_tile(p0, p1, qm - kb, 0x7fffffffu);
.LBB0_324:
	s_add_i32 s4, s5, -1
	s_and_b32 s20, s4, 1
	s_lshl_b32 s4, s20, 14
	v_add3_u32 v245, s4, v206, v205
	v_add3_u32 v242, s4, v207, v205
	v_add3_u32 v243, s4, v208, v205
	v_add3_u32 v244, s4, v209, v205
	ds_read_b128 v[214:217], v245
	ds_read_b128 v[218:221], v242
	ds_read_b128 v[130:133], v245 offset:8192
	ds_read_b128 v[222:225], v242 offset:8192
	ds_read_b128 v[226:229], v243
	ds_read_b128 v[230:233], v243 offset:8192
	ds_read_b128 v[234:237], v244
	ds_read_b128 v[238:241], v244 offset:8192
	s_cmp_lt_u32 s19, 0x2000
	s_cbranch_scc0 .Latt_x_noload
	s_cmp_lt_u32 s5, s57
	s_cbranch_scc0 .Latt_x_noload
	s_xor_b32 s21, s4, 0x4000
	s_add_i32 s21, s19, s21
	s_lshl_b32 s64, s20, 15
	s_xor_b32 s64, s64, 0x8000
	s_add_i32 s64, s19, s64
	s_add_u32 s60, s58, s25
	s_addc_u32 s61, s59, s22
	s_mov_b32 m0, s21
	s_nop 0
	global_load_lds_dwordx4 v199, s[60:61]
	s_add_i32 m0, s21, 0x400
	s_nop 0
	global_load_lds_dwordx4 v200, s[60:61]
	s_add_u32 s60, s58, s52
	s_addc_u32 s61, s59, s53
	v_mov_b32_e32 v0, v201
	v_lshl_add_u64 v[146:147], s[60:61], 0, v[0:1]
	v_lshl_add_u64 v[148:149], v[146:147], 0, s[42:43]
	s_add_i32 m0, s64, 0x8000
	v_lshl_add_u64 v[146:147], v[146:147], 0, s[44:45]
	global_load_lds_dwordx4 v[148:149], off
	s_add_i32 m0, s64, 0xc000
	v_mov_b32_e32 v0, v202
	global_load_lds_dwordx4 v[146:147], off
	v_lshl_add_u64 v[146:147], s[60:61], 0, v[0:1]
	v_lshl_add_u64 v[148:149], v[146:147], 0, s[42:43]
	s_add_i32 m0, s64, 0x8400
	v_lshl_add_u64 v[146:147], v[146:147], 0, s[44:45]
	global_load_lds_dwordx4 v[148:149], off
	s_add_i32 m0, s64, 0xc400
	s_nop 0
	global_load_lds_dwordx4 v[146:147], off
.Latt_x_noload:
	s_waitcnt lgkmcnt(7)
	v_mfma_f32_32x32x16_bf16 v[146:161], v[214:217], v[162:165], 0
	ds_read_b128 v[214:217], v245 offset:128
	s_waitcnt lgkmcnt(7)
	v_mfma_f32_32x32x16_bf16 v[146:161], v[218:221], v[166:169], v[146:161]
	ds_read_b128 v[218:221], v245 offset:8320
	s_waitcnt lgkmcnt(7)
	v_mfma_f32_32x32x16_bf16 v[130:145], v[130:133], v[162:165], 0
	s_waitcnt lgkmcnt(6)
	v_mfma_f32_32x32x16_bf16 v[130:145], v[222:225], v[166:169], v[130:145]
	ds_read_b128 v[222:225], v242 offset:128
	s_waitcnt lgkmcnt(6)
	v_mfma_f32_32x32x16_bf16 v[146:161], v[226:229], v[170:173], v[146:161]
	ds_read_b128 v[226:229], v242 offset:8320
	s_waitcnt lgkmcnt(6)
	v_mfma_f32_32x32x16_bf16 v[130:145], v[230:233], v[170:173], v[130:145]
	ds_read_b128 v[230:233], v243 offset:128
	s_waitcnt lgkmcnt(6)
	v_mfma_f32_32x32x16_bf16 v[146:161], v[234:237], v[174:177], v[146:161]
	ds_read_b128 v[234:237], v243 offset:8320
	s_waitcnt lgkmcnt(6)
	v_mfma_f32_32x32x16_bf16 v[130:145], v[238:241], v[174:177], v[130:145]
	ds_read_b128 v[238:241], v244 offset:128
	s_waitcnt lgkmcnt(6)
	v_mfma_f32_32x32x16_bf16 v[146:161], v[214:217], v[178:181], v[146:161]
	ds_read_b128 v[214:217], v244 offset:8320
	s_waitcnt lgkmcnt(6)
	v_mfma_f32_32x32x16_bf16 v[130:145], v[218:221], v[178:181], v[130:145]
	s_waitcnt lgkmcnt(5)
	v_mfma_f32_32x32x16_bf16 v[146:161], v[222:225], v[182:185], v[146:161]
	s_waitcnt lgkmcnt(4)
	v_mfma_f32_32x32x16_bf16 v[130:145], v[226:229], v[182:185], v[130:145]
	s_waitcnt lgkmcnt(3)
	v_mfma_f32_32x32x16_bf16 v[146:161], v[230:233], v[186:189], v[146:161]
	s_waitcnt lgkmcnt(2)
	v_mfma_f32_32x32x16_bf16 v[130:145], v[234:237], v[186:189], v[130:145]
	s_waitcnt lgkmcnt(1)
	v_mfma_f32_32x32x16_bf16 v[146:161], v[238:241], v[190:193], v[146:161]
	s_waitcnt lgkmcnt(0)
	v_mfma_f32_32x32x16_bf16 v[130:145], v[214:217], v[190:193], v[130:145]
	s_cmp_lt_u32 s19, 0x2000
	s_cbranch_scc1 .Latt_l2_skip
	s_cmp_lt_u32 s5, s57
	s_cbranch_scc0 .Latt_l2_skip
	s_lshl_b32 s21, s20, 14
	s_xor_b32 s21, s21, 0x4000
	s_add_i32 s21, s19, s21
	s_lshl_b32 s64, s20, 15
	s_xor_b32 s64, s64, 0x8000
	s_add_i32 s64, s19, s64
	v_mov_b32_e32 v233, 0
	s_add_u32 s60, s58, s25
	s_addc_u32 s61, s59, s22
	s_mov_b32 m0, s21
	s_nop 0
	global_load_lds_dwordx4 v199, s[60:61]
	s_add_i32 m0, s21, 0x400
	s_nop 0
	global_load_lds_dwordx4 v200, s[60:61]
	s_add_u32 s60, s58, s52
	s_addc_u32 s61, s59, s53
	v_mov_b32_e32 v232, v201
	v_lshl_add_u64 v[234:235], s[60:61], 0, v[232:233]
	v_lshl_add_u64 v[236:237], v[234:235], 0, s[42:43]
	s_add_i32 m0, s64, 0x8000
	v_lshl_add_u64 v[234:235], v[234:235], 0, s[44:45]
	global_load_lds_dwordx4 v[236:237], off
	s_add_i32 m0, s64, 0xc000
	v_mov_b32_e32 v232, v202
	global_load_lds_dwordx4 v[234:235], off
	v_lshl_add_u64 v[234:235], s[60:61], 0, v[232:233]
	v_lshl_add_u64 v[236:237], v[234:235], 0, s[42:43]
	s_add_i32 m0, s64, 0x8400
	v_lshl_add_u64 v[234:235], v[234:235], 0, s[44:45]
	global_load_lds_dwordx4 v[236:237], off
	s_add_i32 m0, s64, 0xc400
	s_nop 0
	global_load_lds_dwordx4 v[234:235], off
; __device__ __forceinline__ void mask_tile(f32x16& p0, f32x16& p1, int dq, unsigned W) {
;     const float NEG = -__builtin_inff();
; #pragma unroll
;     for (int r = 0; r < 16; ++r) {
;         const int c = (r & 3) + 8 * (r >> 2);
;         if ((unsigned)(dq - c) >= W) p0[r] = NEG;
;         if ((unsigned)(dq - c - 32) >= W) p1[r] = NEG;
;     }
; }
; __device__ __forceinline__ void block(const Blk& B, char* lds, A3_LAS unsigned char* ldsl, const int tid) {
;     ...
;         if (kb + 63 > qlo) attn::mask_tile(p0, p1, qm - kb, 0x7fffffffu);
.Latt_l2_skip:
	s_add_i32 s4, s62, 0x13f
	s_cmp_le_i32 s4, s23
	s_cbranch_scc1 .LBB0_330
	v_add_u32_e32 v0, s17, v211
	s_brev_b32 s4, -2
	v_cmp_gt_u32_e32 vcc, s4, v0
	v_add_u32_e32 v214, 0x7fffffe1, v0
	s_nop 3
	v_cndmask_b32_e32 v146, v195, v146, vcc
	v_cmp_lt_u32_e32 vcc, s91, v214
	v_add_u32_e32 v214, 0x7fffffe0, v0
	s_nop 0
	v_cndmask_b32_e32 v130, v195, v130, vcc
	v_cmp_lt_i32_e32 vcc, 0, v0
	s_nop 1
	v_cndmask_b32_e32 v147, v195, v147, vcc
	v_cmp_lt_u32_e32 vcc, s91, v214
	v_add_u32_e32 v214, 0x7fffffff, v0
	s_nop 0
	v_cndmask_b32_e32 v131, v195, v131, vcc
	v_cmp_lt_u32_e32 vcc, s91, v214
	v_add_u32_e32 v214, 0x7fffffdf, v0
	s_nop 0
	v_cndmask_b32_e32 v148, v195, v148, vcc
	v_cmp_lt_u32_e32 vcc, s91, v214
	v_add_u32_e32 v214, 0x7ffffffe, v0
	s_nop 0
	v_cndmask_b32_e32 v132, v195, v132, vcc
	v_cmp_lt_u32_e32 vcc, s91, v214
	v_add_u32_e32 v214, 0x7fffffde, v0
	s_nop 0
	v_cndmask_b32_e32 v149, v195, v149, vcc
	v_cmp_lt_u32_e32 vcc, s91, v214
	v_add_u32_e32 v214, 0x7ffffff9, v0
	s_nop 0
	v_cndmask_b32_e32 v133, v195, v133, vcc
	v_cmp_lt_u32_e32 vcc, s91, v214
	v_add_u32_e32 v214, 0x7fffffd9, v0
	s_nop 0
	v_cndmask_b32_e32 v150, v195, v150, vcc
	v_cmp_lt_u32_e32 vcc, s91, v214
	v_add_u32_e32 v214, 0x7ffffff8, v0
	s_nop 0
	v_cndmask_b32_e32 v134, v195, v134, vcc
	v_cmp_lt_u32_e32 vcc, s91, v214
	v_add_u32_e32 v214, 0x7fffffd8, v0
	s_nop 0
	v_cndmask_b32_e32 v151, v195, v151, vcc
	v_cmp_lt_u32_e32 vcc, s91, v214
	v_add_u32_e32 v214, 0x7ffffff7, v0
	s_nop 0
	v_cndmask_b32_e32 v135, v195, v135, vcc
	v_cmp_lt_u32_e32 vcc, s91, v214
	v_add_u32_e32 v214, 0x7fffffd7, v0
	s_nop 0
	v_cndmask_b32_e32 v152, v195, v152, vcc
	v_cmp_lt_u32_e32 vcc, s91, v214
	v_add_u32_e32 v214, 0x7ffffff6, v0
	s_nop 0
	v_cndmask_b32_e32 v136, v195, v136, vcc
	v_cmp_lt_u32_e32 vcc, s91, v214
	v_add_u32_e32 v214, 0x7fffffd6, v0
	s_nop 0
	v_cndmask_b32_e32 v153, v195, v153, vcc
	v_cmp_lt_u32_e32 vcc, s91, v214
	v_add_u32_e32 v214, 0x7ffffff1, v0
	s_nop 0
	v_cndmask_b32_e32 v137, v195, v137, vcc
	v_cmp_lt_u32_e32 vcc, s91, v214
	v_add_u32_e32 v214, 0x7fffffd1, v0
	s_nop 0
	v_cndmask_b32_e32 v154, v195, v154, vcc
	v_cmp_lt_u32_e32 vcc, s91, v214
	v_add_u32_e32 v214, 0x7ffffff0, v0
	s_nop 0
	v_cndmask_b32_e32 v138, v195, v138, vcc
	v_cmp_lt_u32_e32 vcc, s91, v214
	v_add_u32_e32 v214, 0x7fffffd0, v0
	s_nop 0
	v_cndmask_b32_e32 v155, v195, v155, vcc
	v_cmp_lt_u32_e32 vcc, s91, v214
	v_add_u32_e32 v214, 0x7fffffef, v0
	s_nop 0
	v_cndmask_b32_e32 v139, v195, v139, vcc
	v_cmp_lt_u32_e32 vcc, s91, v214
	v_add_u32_e32 v214, 0x7fffffcf, v0
	s_nop 0
	v_cndmask_b32_e32 v156, v195, v156, vcc
	v_cmp_lt_u32_e32 vcc, s91, v214
	v_add_u32_e32 v214, 0x7fffffee, v0
	s_nop 0
	v_cndmask_b32_e32 v140, v195, v140, vcc
	v_cmp_lt_u32_e32 vcc, s91, v214
	v_add_u32_e32 v214, 0x7fffffce, v0
	s_nop 0
	v_cndmask_b32_e32 v157, v195, v157, vcc
	v_cmp_lt_u32_e32 vcc, s91, v214
	v_add_u32_e32 v214, 0x7fffffe9, v0
	s_nop 0
	v_cndmask_b32_e32 v141, v195, v141, vcc
	v_cmp_lt_u32_e32 vcc, s91, v214
	v_add_u32_e32 v214, 0x7fffffc9, v0
	s_nop 0
	v_cndmask_b32_e32 v158, v195, v158, vcc
	v_cmp_lt_u32_e32 vcc, s91, v214
	v_add_u32_e32 v214, 0x7fffffe8, v0
	s_nop 0
	v_cndmask_b32_e32 v142, v195, v142, vcc
	v_cmp_lt_u32_e32 vcc, s91, v214
	v_add_u32_e32 v214, 0x7fffffc8, v0
	s_nop 0
	v_cndmask_b32_e32 v159, v195, v159, vcc
	v_cmp_lt_u32_e32 vcc, s91, v214
	v_add_u32_e32 v214, 0x7fffffe7, v0
	s_nop 0
	v_cndmask_b32_e32 v143, v195, v143, vcc
	v_cmp_lt_u32_e32 vcc, s91, v214
	v_add_u32_e32 v214, 0x7fffffc7, v0
	s_nop 0
	v_cndmask_b32_e32 v160, v195, v160, vcc
	v_cmp_lt_u32_e32 vcc, s91, v214
	v_add_u32_e32 v214, 0x7fffffe6, v0
	v_add_u32_e32 v0, 0x7fffffc6, v0
	v_cndmask_b32_e32 v144, v195, v144, vcc
	v_cmp_lt_u32_e32 vcc, s91, v214
	s_nop 1
	v_cndmask_b32_e32 v161, v195, v161, vcc
	v_cmp_lt_u32_e32 vcc, s91, v0
	s_nop 1
	v_cndmask_b32_e32 v145, v195, v145, vcc

; #define A3_RDK(vb, d0, s) do { A3_TRRD(xl##s, vb, (d0) * 512 + (s) * 4096); A3_TRRD(xh##s, vb, (d0) * 512 + (s) * 4096 + 2048); A3_TRRD(yl##s, vb, ((d0) + 1) * 512 + (s) * 4096); A3_TRRD(yh##s, vb, ((d0) + 1) * 512 + (s) * 4096 + 2048); } while (0)
; #define A3_PAIR(accx, accy, NEXT0, NEXT1, NEXT2, NEXT3) do { A3_STEPK(accx, accy, pa0, 0, NEXT0); A3_STEPK(accx, accy, pa1, 1, NEXT1); A3_STEPK(accx, accy, pa2, 2, NEXT2); A3_STEPK(accx, accy, pa3, 3, NEXT3); } while (0)
; #define A3_NONE do { asm volatile("s_waitcnt lgkmcnt(0)" ::: "memory"); } while (0)
; __device__ __forceinline__ float own_sum(const f32x16& P) { return ((P[0] + P[1]) + (P[2] + P[3])) + ((P[4] + P[5]) + (P[6] + P[7])) + (((P[8] + P[9]) + (P[10] + P[11])) + ((P[12] + P[13]) + (P[14] + P[15]))); }
; __device__ __forceinline__ void pv256(f32x16* o, int vb0, bf16x8 pa0, bf16x8 pa1, bf16x8 pa2, bf16x8 pa3) {
;     s16x4 xl0, xh0, xl1, xh1, xl2, xh2, xl3, xh3, yl0, yh0, yl1, yh1, yl2, yh2, yl3, yh3;
;     const int va = vb0, vb = vb0 + 16384;
;     asm volatile("s_waitcnt lgkmcnt(0)" ::: "memory");
;     A3_RDK(va, 0, 0); A3_RDK(va, 0, 1); A3_RDK(va, 0, 2); A3_RDK(va, 0, 3);
;     A3_PAIR(o[0], o[1], A3_RDK(va, 2, 0), A3_RDK(va, 2, 1), A3_RDK(va, 2, 2), A3_RDK(va, 2, 3));
;     A3_PAIR(o[2], o[3], A3_RDK(vb, 0, 0), A3_RDK(vb, 0, 1), A3_RDK(vb, 0, 2), A3_RDK(vb, 0, 3));
;     A3_PAIR(o[4], o[5], A3_RDK(vb, 2, 0), A3_RDK(vb, 2, 1), A3_RDK(vb, 2, 2), A3_RDK(vb, 2, 3));
;     A3_PAIR(o[6], o[7], A3_NONE, A3_NONE, A3_NONE, A3_NONE);
; }
; __device__ __forceinline__ void block(const Blk& B, char* lds, A3_LAS unsigned char* ldsl, const int tid) {
;     ...
;         l_reg = l_reg * alpha + (own_sum(p0) + own_sum(p1));
;     ...
;         pv256(o, vb0 + buf * 32768, pa0, pa1, pa2, pa3);
.LBB0_336:
	v_add_f32_e32 v146, v217, v219
	v_add_f32_e32 v147, v221, v223
	v_add_f32_e32 v146, v146, v147
	v_add_f32_e32 v147, v226, v228
	v_add_f32_e32 v148, v230, v232
	v_add_f32_e32 v147, v147, v148
	v_add_f32_e32 v146, v146, v147
	v_add_f32_e32 v147, v233, v235
	v_add_f32_e32 v148, v238, v240
	v_add_f32_e32 v147, v147, v148
	v_add_f32_e32 v148, v242, v243
	v_add_f32_e32 v149, v244, v245
	v_add_f32_e32 v148, v148, v149
	v_add_f32_e32 v147, v147, v148
	v_add_f32_e32 v146, v146, v147
	v_add_f32_e32 v147, v213, v214
	v_add_f32_e32 v148, v215, v216
	v_add_f32_e32 v147, v147, v148
	v_add_f32_e32 v148, v218, v220
	v_add_f32_e32 v149, v222, v224
	v_add_f32_e32 v148, v148, v149
	v_add_f32_e32 v147, v147, v148
	v_add_f32_e32 v148, v225, v227
	v_add_f32_e32 v149, v229, v231
	v_add_f32_e32 v148, v148, v149
	v_add_f32_e32 v149, v234, v236
	v_add_f32_e32 v150, v239, v241
	v_add_f32_e32 v149, v149, v150
	v_add_f32_e32 v148, v148, v149
	v_add_f32_e32 v147, v147, v148
	s_waitcnt lgkmcnt(0)
	v_add_f32_e32 v146, v147, v146
	v_lshl_add_u32 v147, s20, 15, v210
	ds_read_b64_tr_b16 v[148:149], v147 offset:0
	ds_read_b64_tr_b16 v[150:151], v147 offset:0x800
	ds_read_b64_tr_b16 v[152:153], v147 offset:0x200
	ds_read_b64_tr_b16 v[154:155], v147 offset:0xa00
	ds_read_b64_tr_b16 v[156:157], v147 offset:0x1000
	ds_read_b64_tr_b16 v[158:159], v147 offset:0x1800
	v_fmac_f32_e32 v146, v212, v237
	ds_read_b64_tr_b16 v[212:213], v147 offset:0x1200
	ds_read_b64_tr_b16 v[214:215], v147 offset:0x1a00
	ds_read_b64_tr_b16 v[216:217], v147 offset:0x2000
	ds_read_b64_tr_b16 v[218:219], v147 offset:0x2800
	ds_read_b64_tr_b16 v[220:221], v147 offset:0x2200
	ds_read_b64_tr_b16 v[222:223], v147 offset:0x2a00
	ds_read_b64_tr_b16 v[224:225], v147 offset:0x3000
	ds_read_b64_tr_b16 v[226:227], v147 offset:0x3800
	ds_read_b64_tr_b16 v[228:229], v147 offset:0x3200
	ds_read_b64_tr_b16 v[230:231], v147 offset:0x3a00
	s_waitcnt lgkmcnt(12)
	v_add_u32_e32 v160, 0x4000, v147
	v_mfma_f32_32x32x16_bf16 v[114:129], v[142:145], v[148:151], v[114:129]
	v_mfma_f32_32x32x16_bf16 v[98:113], v[142:145], v[152:155], v[98:113]
	ds_read_b64_tr_b16 v[148:149], v147 offset:0x400
	ds_read_b64_tr_b16 v[150:151], v147 offset:0xc00
	ds_read_b64_tr_b16 v[152:153], v147 offset:0x600
	ds_read_b64_tr_b16 v[154:155], v147 offset:0xe00
	s_waitcnt lgkmcnt(12)
	v_mfma_f32_32x32x16_bf16 v[114:129], v[138:141], v[156:159], v[114:129]
	v_mfma_f32_32x32x16_bf16 v[98:113], v[138:141], v[212:215], v[98:113]
	ds_read_b64_tr_b16 v[156:157], v147 offset:0x1400
	ds_read_b64_tr_b16 v[158:159], v147 offset:0x1c00
	ds_read_b64_tr_b16 v[212:213], v147 offset:0x1600
	ds_read_b64_tr_b16 v[214:215], v147 offset:0x1e00
	s_waitcnt lgkmcnt(12)
	v_mfma_f32_32x32x16_bf16 v[114:129], v[134:137], v[216:219], v[114:129]
	v_mfma_f32_32x32x16_bf16 v[98:113], v[134:137], v[220:223], v[98:113]
	ds_read_b64_tr_b16 v[216:217], v147 offset:0x2400
	ds_read_b64_tr_b16 v[218:219], v147 offset:0x2c00
	ds_read_b64_tr_b16 v[220:221], v147 offset:0x2600
	ds_read_b64_tr_b16 v[222:223], v147 offset:0x2e00
	s_waitcnt lgkmcnt(12)
	v_mfma_f32_32x32x16_bf16 v[114:129], v[130:133], v[224:227], v[114:129]
	v_mfma_f32_32x32x16_bf16 v[98:113], v[130:133], v[228:231], v[98:113]
	ds_read_b64_tr_b16 v[224:225], v147 offset:0x3400
	ds_read_b64_tr_b16 v[226:227], v147 offset:0x3c00
	ds_read_b64_tr_b16 v[228:229], v147 offset:0x3600
	ds_read_b64_tr_b16 v[230:231], v147 offset:0x3e00
	s_waitcnt lgkmcnt(12)
	v_mfma_f32_32x32x16_bf16 v[82:97], v[142:145], v[148:151], v[82:97]
	v_mfma_f32_32x32x16_bf16 v[66:81], v[142:145], v[152:155], v[66:81]
	ds_read_b64_tr_b16 v[148:149], v160 offset:0
	ds_read_b64_tr_b16 v[150:151], v160 offset:0x800
	ds_read_b64_tr_b16 v[152:153], v160 offset:0x200
	ds_read_b64_tr_b16 v[154:155], v160 offset:0xa00
	s_waitcnt lgkmcnt(12)
; #define A3_RDK(vb, d0, s) do { A3_TRRD(xl##s, vb, (d0) * 512 + (s) * 4096); A3_TRRD(xh##s, vb, (d0) * 512 + (s) * 4096 + 2048); A3_TRRD(yl##s, vb, ((d0) + 1) * 512 + (s) * 4096); A3_TRRD(yh##s, vb, ((d0) + 1) * 512 + (s) * 4096 + 2048); } while (0)
; #define A3_PAIR(accx, accy, NEXT0, NEXT1, NEXT2, NEXT3) do { A3_STEPK(accx, accy, pa0, 0, NEXT0); A3_STEPK(accx, accy, pa1, 1, NEXT1); A3_STEPK(accx, accy, pa2, 2, NEXT2); A3_STEPK(accx, accy, pa3, 3, NEXT3); } while (0)
; #define A3_NONE do { asm volatile("s_waitcnt lgkmcnt(0)" ::: "memory"); } while (0)
; __device__ __forceinline__ void pv256(f32x16* o, int vb0, bf16x8 pa0, bf16x8 pa1, bf16x8 pa2, bf16x8 pa3) {
;     ...
;     A3_PAIR(o[0], o[1], A3_RDK(va, 2, 0), A3_RDK(va, 2, 1), A3_RDK(va, 2, 2), A3_RDK(va, 2, 3));
;     A3_PAIR(o[2], o[3], A3_RDK(vb, 0, 0), A3_RDK(vb, 0, 1), A3_RDK(vb, 0, 2), A3_RDK(vb, 0, 3));
;     A3_PAIR(o[4], o[5], A3_RDK(vb, 2, 0), A3_RDK(vb, 2, 1), A3_RDK(vb, 2, 2), A3_RDK(vb, 2, 3));
;     A3_PAIR(o[6], o[7], A3_NONE, A3_NONE, A3_NONE, A3_NONE);
; __device__ __forceinline__ void block(const Blk& B, char* lds, A3_LAS unsigned char* ldsl, const int tid) {
;     ...
;         pv256(o, vb0 + buf * 32768, pa0, pa1, pa2, pa3);
;         asm volatile("s_waitcnt vmcnt(0)" ::: "memory");
;         __syncthreads();
;     }
	v_mfma_f32_32x32x16_bf16 v[82:97], v[138:141], v[156:159], v[82:97]
	v_mfma_f32_32x32x16_bf16 v[66:81], v[138:141], v[212:215], v[66:81]
	ds_read_b64_tr_b16 v[156:157], v160 offset:0x1000
	ds_read_b64_tr_b16 v[158:159], v160 offset:0x1800
	ds_read_b64_tr_b16 v[212:213], v160 offset:0x1200
	ds_read_b64_tr_b16 v[214:215], v160 offset:0x1a00
	s_waitcnt lgkmcnt(12)
	v_mfma_f32_32x32x16_bf16 v[82:97], v[134:137], v[216:219], v[82:97]
	v_mfma_f32_32x32x16_bf16 v[66:81], v[134:137], v[220:223], v[66:81]
	ds_read_b64_tr_b16 v[216:217], v160 offset:0x2000
	ds_read_b64_tr_b16 v[218:219], v160 offset:0x2800
	ds_read_b64_tr_b16 v[220:221], v160 offset:0x2200
	ds_read_b64_tr_b16 v[222:223], v160 offset:0x2a00
	s_waitcnt lgkmcnt(12)
	v_mfma_f32_32x32x16_bf16 v[82:97], v[130:133], v[224:227], v[82:97]
	v_mfma_f32_32x32x16_bf16 v[66:81], v[130:133], v[228:231], v[66:81]
	ds_read_b64_tr_b16 v[224:225], v160 offset:0x3000
	ds_read_b64_tr_b16 v[226:227], v160 offset:0x3800
	ds_read_b64_tr_b16 v[228:229], v160 offset:0x3200
	ds_read_b64_tr_b16 v[230:231], v160 offset:0x3a00
	s_waitcnt lgkmcnt(12)
	v_mfma_f32_32x32x16_bf16 v[50:65], v[142:145], v[148:151], v[50:65]
	v_mfma_f32_32x32x16_bf16 v[34:49], v[142:145], v[152:155], v[34:49]
	ds_read_b64_tr_b16 v[148:149], v160 offset:0x400
	ds_read_b64_tr_b16 v[150:151], v160 offset:0xc00
	ds_read_b64_tr_b16 v[152:153], v160 offset:0x600
	ds_read_b64_tr_b16 v[154:155], v160 offset:0xe00
	s_waitcnt lgkmcnt(12)
	v_mfma_f32_32x32x16_bf16 v[50:65], v[138:141], v[156:159], v[50:65]
	v_mfma_f32_32x32x16_bf16 v[34:49], v[138:141], v[212:215], v[34:49]
	ds_read_b64_tr_b16 v[156:157], v160 offset:0x1400
	ds_read_b64_tr_b16 v[158:159], v160 offset:0x1c00
	ds_read_b64_tr_b16 v[212:213], v160 offset:0x1600
	ds_read_b64_tr_b16 v[214:215], v160 offset:0x1e00
	s_waitcnt lgkmcnt(12)
	v_mfma_f32_32x32x16_bf16 v[50:65], v[134:137], v[216:219], v[50:65]
	v_mfma_f32_32x32x16_bf16 v[34:49], v[134:137], v[220:223], v[34:49]
	ds_read_b64_tr_b16 v[216:217], v160 offset:0x2400
	ds_read_b64_tr_b16 v[218:219], v160 offset:0x2c00
	ds_read_b64_tr_b16 v[220:221], v160 offset:0x2600
	ds_read_b64_tr_b16 v[222:223], v160 offset:0x2e00
	s_waitcnt lgkmcnt(12)
	v_mfma_f32_32x32x16_bf16 v[50:65], v[130:133], v[224:227], v[50:65]
	v_mfma_f32_32x32x16_bf16 v[34:49], v[130:133], v[228:231], v[34:49]
	ds_read_b64_tr_b16 v[224:225], v160 offset:0x3400
	ds_read_b64_tr_b16 v[226:227], v160 offset:0x3c00
	ds_read_b64_tr_b16 v[228:229], v160 offset:0x3600
	ds_read_b64_tr_b16 v[230:231], v160 offset:0x3e00
	s_waitcnt lgkmcnt(12)
	v_mfma_f32_32x32x16_bf16 v[18:33], v[142:145], v[148:151], v[18:33]
	v_mfma_f32_32x32x16_bf16 v[2:17], v[142:145], v[152:155], v[2:17]
	s_waitcnt lgkmcnt(0)
	s_waitcnt lgkmcnt(12)
	v_mfma_f32_32x32x16_bf16 v[18:33], v[138:141], v[156:159], v[18:33]
	v_mfma_f32_32x32x16_bf16 v[2:17], v[138:141], v[212:215], v[2:17]
	s_waitcnt lgkmcnt(0)
	s_waitcnt lgkmcnt(12)
	v_mfma_f32_32x32x16_bf16 v[18:33], v[134:137], v[216:219], v[18:33]
	v_mfma_f32_32x32x16_bf16 v[2:17], v[134:137], v[220:223], v[2:17]
	s_waitcnt lgkmcnt(0)
	s_waitcnt lgkmcnt(12)
	v_mfma_f32_32x32x16_bf16 v[18:33], v[130:133], v[224:227], v[18:33]
	v_mfma_f32_32x32x16_bf16 v[2:17], v[130:133], v[228:231], v[2:17]
	s_waitcnt lgkmcnt(0)
	s_waitcnt vmcnt(0)
	s_add_u32 s58, s58, 0x4000
	s_addc_u32 s59, s59, 0
	s_add_i32 s62, s62, 64
	s_add_i32 s5, s5, 1
	v_subrev_u32_e32 v211, 64, v211
	s_cmp_eq_u32 s17, s62
	s_barrier
	s_cbranch_scc1 .LBB0_338
	v_mov_b32_e32 v213, v0
	v_mov_b32_e32 v212, v146
	s_branch .LBB0_324
